# attention: V fragments for c-blocks 2,3 read before QK MFMAs, PV starts with those blocks
# speedup vs baseline: 1.0135x; 1.0043x over previous
.LBB0_397:
	s_add_i32 s0, s34, 0x80
	s_cmp_le_u32 s0, s24
	s_cselect_b64 s[78:79], -1, 0
	s_add_i32 s82, s31, 0
	s_add_i32 s3, s34, 0x13f
	s_cmp_gt_u32 s3, s16
	s_cselect_b64 s[36:37], -1, 0
	s_cmp_gt_u32 s0, s24
	s_cbranch_scc1 .Latt_noqk
	v_add_u32_e32 v152, s82, v164
	ds_read_b128 v[204:207], v152
	ds_read_b128 v[208:211], v152 offset:512
	ds_read_b128 v[212:215], v152 offset:2048
	ds_read_b128 v[216:219], v152 offset:2560
	s_add_i32 s0, s73, 0
	v_add_u32_e32 v196, s0, v171
	v_add_u32_e32 v197, s0, v170
	v_add_u32_e32 v202, s0, v169
	v_add_u32_e32 v203, s0, v168
	ds_read_b64_tr_b16 v[178:179], v196 offset:16384
	ds_read_b64_tr_b16 v[180:181], v197 offset:16384
	ds_read_b64_tr_b16 v[184:185], v197 offset:20480
	ds_read_b64_tr_b16 v[182:183], v196 offset:20480
	ds_read_b64_tr_b16 v[186:187], v202 offset:16384
	ds_read_b64_tr_b16 v[188:189], v203 offset:16384
	ds_read_b64_tr_b16 v[192:193], v203 offset:20480
	ds_read_b64_tr_b16 v[190:191], v202 offset:20480
	v_cndmask_b32_e64 v68, v165, 0, s[36:37]
	v_sub_f32_e32 v68, v68, v167
	v_mov_b32_e32 v82, v68
	v_mov_b32_e32 v83, v68
	v_mov_b32_e32 v69, v68
	v_mov_b32_e32 v70, v68
	v_mov_b32_e32 v71, v68
	v_mov_b32_e32 v72, v68
	v_mov_b32_e32 v73, v68
	v_mov_b32_e32 v74, v68
	v_mov_b32_e32 v75, v68
	v_mov_b32_e32 v76, v68
	v_mov_b32_e32 v77, v68
	v_mov_b32_e32 v78, v68
	v_mov_b32_e32 v79, v68
	v_mov_b32_e32 v80, v68
	v_mov_b32_e32 v81, v68
	s_nop 1
	s_waitcnt lgkmcnt(11)
	v_mfma_f32_32x32x16_bf16 v[100:115], v[204:207], v[116:119], v[68:83]
	s_waitcnt lgkmcnt(10)
	v_mfma_f32_32x32x16_bf16 v[84:99], v[208:211], v[116:119], v[68:83]
	s_waitcnt lgkmcnt(9)
	v_mfma_f32_32x32x16_bf16 v[100:115], v[212:215], v[120:123], v[100:115]
	ds_read_b128 v[204:207], v152 offset:4096
	ds_read_b128 v[208:211], v152 offset:4608
	ds_read_b128 v[212:215], v152 offset:6144
	s_waitcnt lgkmcnt(11)
	v_mfma_f32_32x32x16_bf16 v[84:99], v[216:219], v[120:123], v[84:99]
	ds_read_b128 v[216:219], v152 offset:6656
	s_waitcnt lgkmcnt(3)
	v_mfma_f32_32x32x16_bf16 v[100:115], v[204:207], v[124:127], v[100:115]
	s_waitcnt lgkmcnt(2)
	v_mfma_f32_32x32x16_bf16 v[84:99], v[208:211], v[124:127], v[84:99]
	s_waitcnt lgkmcnt(1)
	v_mfma_f32_32x32x16_bf16 v[68:83], v[212:215], v[128:131], v[100:115]
	s_waitcnt lgkmcnt(0)
	v_mfma_f32_32x32x16_bf16 v[84:99], v[216:219], v[128:131], v[84:99]
	s_andn2_b64 vcc, exec, s[36:37]
	s_cbranch_vccnz .LBB0_432
	v_add_u32_e32 v177, s5, v176
	s_mov_b32 s100, 0x207a4
	v_lshl_add_u32 v177, v177, 2, s100
	ds_read2_b32 v[204:205], v177 offset0:55 offset1:54
	ds_read2_b32 v[206:207], v177 offset0:53 offset1:52
	ds_read2_b32 v[208:209], v177 offset0:51 offset1:50
	ds_read2_b32 v[210:211], v177 offset0:49 offset1:48
	ds_read2_b32 v[212:213], v177 offset0:39 offset1:38
	ds_read2_b32 v[214:215], v177 offset0:37 offset1:36
	ds_read2_b32 v[216:217], v177 offset0:35 offset1:34
	ds_read2_b32 v[218:219], v177 offset0:33 offset1:32
	ds_read2_b32 v[220:221], v177 offset0:23 offset1:22
	ds_read2_b32 v[222:223], v177 offset0:21 offset1:20
	ds_read2_b32 v[224:225], v177 offset0:19 offset1:18
	ds_read2_b32 v[226:227], v177 offset0:17 offset1:16
	ds_read2_b32 v[228:229], v177 offset0:7 offset1:6
	ds_read2_b32 v[230:231], v177 offset0:5 offset1:4
	ds_read2_b32 v[232:233], v177 offset0:3 offset1:2
	s_waitcnt lgkmcnt(14)
	v_pk_add_f32 v[68:69], v[68:69], v[204:205]
	ds_read2_b32 v[204:205], v177 offset0:1 offset1:0
	s_waitcnt lgkmcnt(8)
	v_pk_add_f32 v[70:71], v[70:71], v[206:207]
	v_pk_add_f32 v[72:73], v[72:73], v[208:209]
	v_pk_add_f32 v[74:75], v[74:75], v[210:211]
	v_pk_add_f32 v[76:77], v[76:77], v[212:213]
	v_pk_add_f32 v[78:79], v[78:79], v[214:215]
	v_pk_add_f32 v[80:81], v[80:81], v[216:217]
	v_pk_add_f32 v[82:83], v[82:83], v[218:219]
	s_waitcnt lgkmcnt(0)
	v_pk_add_f32 v[84:85], v[84:85], v[220:221]
	v_pk_add_f32 v[86:87], v[86:87], v[222:223]
	v_pk_add_f32 v[88:89], v[88:89], v[224:225]
	v_pk_add_f32 v[90:91], v[90:91], v[226:227]
	v_pk_add_f32 v[92:93], v[92:93], v[228:229]
	v_pk_add_f32 v[94:95], v[94:95], v[230:231]
	v_pk_add_f32 v[96:97], v[96:97], v[232:233]
	v_pk_add_f32 v[98:99], v[98:99], v[204:205]

.Latt_noqk:
	v_cndmask_b32_e64 v68, v165, 0, s[36:37]
	v_sub_f32_e32 v68, v68, v167
	v_mov_b32_e32 v82, v68
	v_mov_b32_e32 v83, v68
	v_mov_b32_e32 v69, v68
	v_mov_b32_e32 v70, v68
	v_mov_b32_e32 v71, v68
	v_mov_b32_e32 v72, v68
	v_mov_b32_e32 v73, v68
	v_mov_b32_e32 v74, v68
	v_mov_b32_e32 v75, v68
	v_mov_b32_e32 v76, v68
	v_mov_b32_e32 v77, v68
	v_mov_b32_e32 v78, v68
	v_mov_b32_e32 v79, v68
	v_mov_b32_e32 v80, v68
	v_mov_b32_e32 v81, v68
	v_mov_b64_e32 v[98:99], v[82:83]
	v_mov_b64_e32 v[96:97], v[80:81]
	v_mov_b64_e32 v[94:95], v[78:79]
	v_mov_b64_e32 v[92:93], v[76:77]
	v_mov_b64_e32 v[90:91], v[74:75]
	v_mov_b64_e32 v[88:89], v[72:73]
	v_mov_b64_e32 v[86:87], v[70:71]
	v_mov_b64_e32 v[84:85], v[68:69]
	s_add_i32 s0, s73, 0
	v_add_u32_e32 v196, s0, v171
	v_add_u32_e32 v197, s0, v170
	v_add_u32_e32 v202, s0, v169
	v_add_u32_e32 v203, s0, v168
	ds_read_b64_tr_b16 v[178:179], v196 offset:16384
	ds_read_b64_tr_b16 v[180:181], v197 offset:16384
	ds_read_b64_tr_b16 v[184:185], v197 offset:20480
	ds_read_b64_tr_b16 v[182:183], v196 offset:20480
	ds_read_b64_tr_b16 v[186:187], v202 offset:16384
	ds_read_b64_tr_b16 v[188:189], v203 offset:16384
	ds_read_b64_tr_b16 v[192:193], v203 offset:20480
	ds_read_b64_tr_b16 v[190:191], v202 offset:20480

.LBB0_435:
	s_add_i32 s0, s73, 0
	v_add_u32_e32 v152, s0, v175
	v_add_u32_e32 v177, s0, v174
	v_add_u32_e32 v194, s0, v173
	v_add_u32_e32 v195, s0, v172
	ds_read_b64_tr_b16 v[100:101], v152 offset:16384
	ds_read_b64_tr_b16 v[102:103], v177 offset:16384
	ds_read_b64_tr_b16 v[106:107], v177 offset:20480
	ds_read_b64_tr_b16 v[104:105], v152 offset:20480
	ds_read_b64_tr_b16 v[108:109], v194 offset:16384
	ds_read_b64_tr_b16 v[110:111], v195 offset:16384
	ds_read_b64_tr_b16 v[114:115], v195 offset:20480
	ds_read_b64_tr_b16 v[112:113], v194 offset:20480
	s_waitcnt lgkmcnt(8)
	v_mfma_f32_32x32x16_bf16 v[20:35], v[178:181], v[144:147], v[20:35]
	v_exp_f32_e32 v68, v68
	v_exp_f32_e32 v69, v69
	v_mfma_f32_32x32x16_bf16 v[4:19], v[186:189], v[144:147], v[4:19]
	v_exp_f32_e32 v70, v70
	v_exp_f32_e32 v71, v71
	v_mfma_f32_32x32x16_bf16 v[20:35], v[182:185], v[140:143], v[20:35]
	v_exp_f32_e32 v72, v72
	v_exp_f32_e32 v73, v73
	v_mfma_f32_32x32x16_bf16 v[4:19], v[190:193], v[140:143], v[4:19]
	v_exp_f32_e32 v74, v74
	v_exp_f32_e32 v75, v75
	s_waitcnt lgkmcnt(6)
	v_mfma_f32_32x32x16_bf16 v[52:67], v[100:103], v[144:147], v[52:67]
	v_exp_f32_e32 v76, v76
	v_exp_f32_e32 v77, v77
	s_waitcnt lgkmcnt(2)
	v_mfma_f32_32x32x16_bf16 v[36:51], v[108:111], v[144:147], v[36:51]
	v_exp_f32_e32 v78, v78
	v_exp_f32_e32 v79, v79
	ds_read_b64_tr_b16 v[100:101], v152 offset:24576
	ds_read_b64_tr_b16 v[102:103], v177 offset:24576
	ds_read_b64_tr_b16 v[108:109], v194 offset:24576
	ds_read_b64_tr_b16 v[110:111], v195 offset:24576
	ds_read_b64_tr_b16 v[178:179], v196 offset:24576
	ds_read_b64_tr_b16 v[180:181], v197 offset:24576
	ds_read_b64_tr_b16 v[186:187], v202 offset:24576
	ds_read_b64_tr_b16 v[188:189], v203 offset:24576
	s_waitcnt lgkmcnt(8)
	v_mfma_f32_32x32x16_bf16 v[52:67], v[104:107], v[140:143], v[52:67]
	v_exp_f32_e32 v80, v80
	v_exp_f32_e32 v81, v81
	v_mfma_f32_32x32x16_bf16 v[36:51], v[112:115], v[140:143], v[36:51]
	v_exp_f32_e32 v82, v82
	v_exp_f32_e32 v83, v83
	ds_read_b64_tr_b16 v[104:105], v152 offset:28672
	ds_read_b64_tr_b16 v[106:107], v177 offset:28672
	ds_read_b64_tr_b16 v[112:113], v194 offset:28672
	ds_read_b64_tr_b16 v[114:115], v195 offset:28672
	ds_read_b64_tr_b16 v[182:183], v196 offset:28672
	ds_read_b64_tr_b16 v[184:185], v197 offset:28672
	ds_read_b64_tr_b16 v[190:191], v202 offset:28672
	ds_read_b64_tr_b16 v[192:193], v203 offset:28672
	s_waitcnt lgkmcnt(14)
	v_mfma_f32_32x32x16_bf16 v[52:67], v[100:103], v[132:135], v[52:67]
	v_exp_f32_e32 v84, v84
	v_exp_f32_e32 v85, v85
	s_waitcnt lgkmcnt(12)
	v_mfma_f32_32x32x16_bf16 v[36:51], v[108:111], v[132:135], v[36:51]
	v_exp_f32_e32 v86, v86
	v_exp_f32_e32 v87, v87
	s_waitcnt lgkmcnt(10)
	v_mfma_f32_32x32x16_bf16 v[20:35], v[178:181], v[132:135], v[20:35]
	v_exp_f32_e32 v88, v88
	v_exp_f32_e32 v89, v89
	s_waitcnt lgkmcnt(8)
	v_mfma_f32_32x32x16_bf16 v[4:19], v[186:189], v[132:135], v[4:19]
	v_exp_f32_e32 v90, v90
	v_exp_f32_e32 v91, v91
	s_waitcnt lgkmcnt(6)
	v_mfma_f32_32x32x16_bf16 v[52:67], v[104:107], v[136:139], v[52:67]
	v_exp_f32_e32 v92, v92
	v_exp_f32_e32 v93, v93
	s_waitcnt lgkmcnt(4)
	v_mfma_f32_32x32x16_bf16 v[36:51], v[112:115], v[136:139], v[36:51]
	v_exp_f32_e32 v94, v94
	v_exp_f32_e32 v95, v95
	s_waitcnt lgkmcnt(2)
	v_mfma_f32_32x32x16_bf16 v[20:35], v[182:185], v[136:139], v[20:35]
	v_exp_f32_e32 v96, v96
	v_exp_f32_e32 v97, v97
	s_waitcnt lgkmcnt(0)
	v_mfma_f32_32x32x16_bf16 v[4:19], v[190:193], v[136:139], v[4:19]
	v_exp_f32_e32 v98, v98
	v_exp_f32_e32 v99, v99
	s_andn2_b64 vcc, exec, s[78:79]
	s_cbranch_vccnz .LBB0_439
